# barrier waits convert with waves 1-5; P11 flush: waves 1-5 finish leftover batches, only waves 1-3 fetch new batches (P13 remap kept)
# speedup vs baseline: 1.0077x; 1.0077x over previous
; __device__ __forceinline__ int lane_id_now() { unsigned z = 0u; asm volatile("" : "+v"(z)); return (int)__builtin_amdgcn_mbcnt_hi(~0u, __builtin_amdgcn_mbcnt_lo(~0u, z)); }
; __device__ __forceinline__ bool cv_one(const CvWork& w) {
;     if (w.wave == 0) return false;
;     int it = __builtin_amdgcn_readfirstlane(w.cur[2 * w.wave]); const int end = __builtin_amdgcn_readfirstlane(w.cur[2 * w.wave + 1]);
;     if (it >= end) {
;         if (it > CV_ITEMS) return false;
;         unsigned base = 0u; if (lane_id_now() == 0) base = __hip_atomic_fetch_add(w.q, (unsigned)CV_BATCH, __ATOMIC_RELAXED, __HIP_MEMORY_SCOPE_AGENT);
;         base = __builtin_amdgcn_readfirstlane(base);
;         if (base >= (unsigned)CV_ITEMS) { w.cur[2 * w.wave] = CV_ITEMS + 1; w.cur[2 * w.wave + 1] = 0; return false; }
;         it = (int)base; w.cur[2 * w.wave + 1] = (int)base + CV_BATCH;
;     }
.LBB0_1416:
	ds_read_b32 v0, v2
	ds_read_b32 v5, v2 offset:4
	s_waitcnt lgkmcnt(1)
	v_readfirstlane_b32 s28, v0
	s_waitcnt lgkmcnt(0)
	v_readfirstlane_b32 s4, v5
	s_cmp_lt_i32 s28, s4
	s_mov_b64 s[4:5], -1
	s_cbranch_scc1 .LBB0_1427
	s_cmp_gt_u32 s89, 3
	s_cbranch_scc1 .LBB0_1430
	s_cmp_lt_i32 s28, 0x10001
	s_mov_b64 s[6:7], 0
	s_cbranch_scc0 .LBB0_1428
	v_mov_b32_e32 v5, 0
	v_mov_b32_e32 v0, 0
	v_mbcnt_lo_u32_b32 v5, -1, v5
	v_mbcnt_hi_u32_b32 v5, -1, v5
	v_cmp_eq_u32_e32 vcc, 0, v5
	s_and_saveexec_b64 s[6:7], vcc
	s_cbranch_execz .LBB0_1422
	s_mov_b64 s[10:11], exec
	v_mbcnt_lo_u32_b32 v0, s10, 0
	v_mbcnt_hi_u32_b32 v0, s11, v0
	v_cmp_eq_u32_e32 vcc, 0, v0
	s_and_saveexec_b64 s[8:9], vcc
	s_cbranch_execz .LBB0_1421
	s_bcnt1_i32_b64 s10, s[10:11]
	s_lshl_b32 s10, s10, 2
	v_mov_b32_e32 v5, s10
	global_atomic_add v5, v1, v5, s[90:91] sc0
